# m11 + rule: when fewer than 29 converter workgroups would fit, take one more GEMM round and use the freed workgroups as converters
# speedup vs baseline: 1.0079x; 1.0079x over previous
; #define LAS __attribute__((address_space(3)))
; __global__ void __launch_bounds__(NTHREADS, 2) fwd(Params p) {
;     ...
;         MoeOrder S{G, bid, 2 * DFF / 256, ntiles, (const LAS unsigned*)(lds + LDS_MISC), (size_t)256 * ND, (size_t)(2 * DFF) * ND, (size_t)256 * ND}; S.ncv = NCV;
;         if (bid < NCV) conv_queue(p, lds, wave, CW_CONV4, N_GU + XP5, N_GU + N_DN - N_DEFER, LDS_MISC + 1024);
.Lncv_p_done:
	s_sub_u32 s98, 0x100, s98
	s_cmp_lt_u32 s98, 29
	s_cbranch_scc0 .Lncv_ok
	s_add_u32 s99, s99, 1
	s_mov_b32 s98, 0xc0

; #define LAS __attribute__((address_space(3)))
; __device__ __forceinline__ void conv_queue(const Params& p, LAS unsigned char* lds, const int wave, const int cw, const int first, const int last, const int slot_off = LDS_MISC) {
;     const int tid = phase_tid(wave);
;     const int lane = tid & 63, wv = tid >> 6;
;     LAS int* slot = (LAS int*)(lds + slot_off);
;     for (;;) {
;         __syncthreads();
;         if (tid == 0) *slot = first + (int)atomicAdd(&p.ctl[cw], 1u);
;         __syncthreads();
;         const int it = *slot;
;         if (it >= last) break;
;         if (it < N_GU) { const int e = it >> 5, rem = it & 31, kb = rem >> 1, nh = rem & 1;
;             const float* src = p.w_gu + (size_t)e * ND * (2 * DFF) + (size_t)(kb * 128) * (2 * DFF) + nh * 2048;
;             fp8_t* dst = p.wt_gu + (size_t)e * (2 * DFF) * ND + (size_t)(nh * 2048) * ND + kb * 128;
;             cvt_item_lds(src, 2 * DFF, dst, ND, lds, tid, wave); }
.Lncv_ok:
	s_cmp_ge_i32 s0, s98
	s_cselect_b64 s[6:7], -1, 0
	s_and_b64 vcc, exec, s[6:7]
	s_cbranch_vccnz .LBB0_1257
	v_mbcnt_lo_u32_b32 v1, -1, 0
	v_mbcnt_hi_u32_b32 v1, -1, v1
	v_readlane_b32 s2, v255, 30
	v_and_b32_e32 v2, 63, v1
	v_add_u32_e32 v3, s91, v1
	v_lshlrev_b32_e32 v0, 2, v2
	v_lshl_add_u32 v6, v2, 9, 0
	v_bitop3_b32 v2, v1, s2, 7 bitop3:0x6c
	v_cmp_eq_u32_e64 s[0:1], 0, v3
	v_lshlrev_b32_e32 v7, 4, v2
	v_ashrrev_i32_e32 v2, 3, v3
	v_lshrrev_b32_e32 v3, 5, v3
	v_xor_b32_e32 v3, v3, v1
	v_lshlrev_b32_e32 v3, 4, v3
	v_add_u32_e32 v4, 64, v2
	v_and_b32_e32 v3, 0x70, v3
	v_ashrrev_i32_e32 v5, 31, v4
	v_add_u32_e32 v8, 0, v3
	v_lshlrev_b32_e32 v1, 4, v1
	v_ashrrev_i32_e32 v3, 31, v2
	v_lshlrev_b32_e32 v9, 7, v4
	v_lshlrev_b64 v[142:143], 11, v[4:5]
	v_add_u32_e32 v4, 0x80, v2
	v_readlane_b32 s16, v254, 5
	v_and_b32_e32 v138, 0x70, v1
	v_lshlrev_b32_e32 v1, 7, v2
	v_lshlrev_b64 v[140:141], 11, v[2:3]
	v_ashrrev_i32_e32 v5, 31, v4
	v_add_u32_e32 v2, 0xc0, v2
	v_readlane_b32 s17, v254, 6
	s_add_u32 s8, s16, 0x20e0
	v_mov_b32_e32 v137, 0
	v_lshlrev_b32_e32 v10, 7, v4
	v_lshlrev_b64 v[144:145], 11, v[4:5]
	v_lshlrev_b32_e32 v4, 7, v2
	v_ashrrev_i32_e32 v3, 31, v2
	s_addc_u32 s9, s17, 0
	s_add_i32 s13, 0, 0x20400
	v_mov_b32_e32 v139, v137
	v_lshlrev_b64 v[146:147], 11, v[2:3]
	v_mov_b32_e32 v204, s13
	s_movk_i32 s60, 0x4000
	s_mov_b32 s61, 0x8000
	s_mov_b32 s62, 0xc000
	s_mov_b32 s63, 0x10000
	s_mov_b32 s64, 0x14000
	s_mov_b32 s65, 0x18000
	s_mov_b32 s66, 0x1c000
	v_add_u32_e32 v205, v6, v7
	v_add_u32_e32 v206, v8, v1
	v_add_u32_e32 v207, v8, v9
	v_add_u32_e32 v208, v8, v10
	v_add_u32_e32 v209, v8, v4
	s_mov_b64 s[10:11], 0x80000
	s_mov_b64 s[38:39], 0x100000
	s_movk_i32 s67, 0x1000
	s_movk_i32 s68, 0x5000
	s_mov_b32 s69, 0x9000
	s_mov_b32 s70, 0xd000
	s_mov_b32 s71, 0x11000
	s_mov_b32 s72, 0x15000
	s_mov_b32 s73, 0x19000
	s_mov_b32 s74, 0x1d000
	s_mov_b64 s[40:41], 0x180000
	s_mov_b64 s[42:43], 0x200000
	s_mov_b64 s[44:45], 0x280000
	s_mov_b64 s[46:47], 0x300000
	s_mov_b64 s[48:49], 0x380000
	v_lshlrev_b32_e32 v136, 2, v0
	v_readlane_b32 s18, v254, 7
	v_readlane_b32 s19, v254, 8
	v_readlane_b32 s20, v254, 9
	v_readlane_b32 s21, v254, 10
	v_readlane_b32 s22, v254, 11
	v_readlane_b32 s23, v254, 12
	v_readlane_b32 s24, v254, 13
	v_readlane_b32 s25, v254, 14
	v_readlane_b32 s26, v254, 15
	v_readlane_b32 s27, v254, 16
	v_readlane_b32 s28, v254, 17
	v_readlane_b32 s29, v254, 18
	v_readlane_b32 s30, v254, 19
	v_readlane_b32 s31, v254, 20
	s_branch .LBB0_1248
